# P1 in-projection GEMM: first K-iteration of every later unit peeled: its two first vmcnt waits leave the previous epilogue stores in flight; C=0 MFMAs replace the accumulator zeroing
# baseline (speedup 1.0000x reference)
; template <unsigned PHMASK> __global__ void __launch_bounds__(NTHR, 2) fwd(Args args) {
;     ...
;         if (PHON(1) && IN(pb + 0)) for (int dup_ = 0; dup_ < ((DUP_PHASE == 1 || DUP_PHASE == 100) ? 2 : 1); ++dup_) { PHASE_FENCE(); pg8::StaticOrder S; S.init((const bf16*)(F.ws + WS_XB), (const bf16*)(lw + LW_IN), T, NZ, DM, F.G, F.bx);
;             pg8::EpiZ E{(bf16*)(F.ws + WS_Z), NZ, Z_MG / 256, (DUP_PHASE == 100) && dup_ == 1};
;             pg8::gemm_phase<pg8::EpiZ, pg8::StaticOrder, false>(F.lds + RING_OFF, DM, S, E, F.tid); }
.LBB0_206:
	s_mul_i32 s0, s8, 11
	s_add_i32 s2, s0, 1
	v_readlane_b32 s4, v249, 5
	v_readlane_b32 s5, v249, 6
	s_cmp_le_i32 s4, s2
	v_writelane_b32 v246, s0, 7
	s_cselect_b64 s[0:1], -1, 0
	s_cmp_lt_i32 s2, s5
	s_cselect_b64 s[2:3], -1, 0
	s_and_b64 s[4:5], s[0:1], s[2:3]
	s_mov_b32 s0, s8
	v_writelane_b32 v246, s0, 8
	s_andn2_b64 vcc, exec, s[4:5]
	s_nop 0
	v_writelane_b32 v246, s1, 9
	s_mul_i32 s0, s8, 0x11600000
	v_writelane_b32 v246, s0, 10
	s_cbranch_vccnz .LBB0_258
	s_mov_b32 s101, 0
	s_mov_b32 s0, -1
	v_readlane_b32 s2, v248, 52
	v_mbcnt_lo_u32_b32 v0, s0, 0
	v_mbcnt_hi_u32_b32 v0, s0, v0
	v_readlane_b32 s0, v249, 4
	v_readlane_b32 s3, v248, 53
	s_andn2_b64 vcc, exec, s[2:3]
	s_waitcnt vmcnt(0)
	v_add_u32_e32 v10, s0, v0
	v_readlane_b32 s0, v247, 30
	s_nop 1
	v_mov_b32_e32 v0, s0
	s_waitcnt lgkmcnt(0)
	ds_read_b64 v[2:3], v0
	v_cmp_ne_u32_e64 s[0:1], 1, v222
	v_readfirstlane_b32 s8, v10
	s_waitcnt lgkmcnt(0)
	v_readfirstlane_b32 s28, v2
	v_readfirstlane_b32 s29, v3
	s_cbranch_vccnz .LBB0_209
	v_readlane_b32 s2, v248, 50
	s_mov_b32 s38, s2
	v_readlane_b32 s2, v248, 51
	s_mov_b32 s48, s2

; template <class Epi, class Sched, bool GATHER, bool SEGHOOK = false>
; __device__ __forceinline__ void gemm_phase(LAS unsigned char* lds, const int K, const Sched& S, const Epi& E, int tid_) {
;     ...
;         const bool has_next = S.next(ui + 1, nxt);
;         const char* nA = has_next ? S.a_base(nxt) : cA; const char* nB = has_next ? S.b_base(nxt) : cB;
; #pragma unroll 1
;         for (int t = 0; t < nt; t += 2) {
;             const bool last = (t == nt - 2);
;             if constexpr (SEGHOOK) { if (t == 16 || t == 32) E.rescale(acc, cur, t >> 4, wr, wc, fr, fq); }
;             const char* a1 = cA + (size_t)(t + 1) * kstep;
;             const char* a2 = last ? nA : cA + (size_t)(t + 2) * kstep; const char* b2 = last ? nB : cB + (size_t)(t + 2) * kstep;
;     ...
; #pragma unroll
;         for (int a = 0; a < 2; ++a)
; #pragma unroll
;             for (int b = 0; b < 2; ++b)
; #pragma unroll
;                 for (int m = 0; m < 4; ++m)
; #pragma unroll
;                     for (int n = 0; n < 2; ++n) acc[a][b][m][n] = (f32x4){0.f, 0.f, 0.f, 0.f};
.LBB0_218:
	s_ashr_i32 s41, s40, 31
	s_lshl_b64 s[8:9], s[40:41], 20
	s_add_u32 s44, s58, s8
	s_addc_u32 s45, s59, s9
	s_and_b64 s[8:9], s[42:43], exec
	s_cselect_b32 s8, s45, s53
	s_cselect_b32 s16, s44, s52
	s_ashr_i32 s13, s12, 31
	s_lshl_b64 s[46:47], s[12:13], 20
	s_add_u32 s46, s60, s46
	s_addc_u32 s47, s61, s47
	s_and_b64 s[54:55], s[42:43], exec
	s_cselect_b32 s13, s47, s51
	s_cselect_b32 s39, s46, s50
	s_add_u32 s41, s50, 0x100
	s_addc_u32 s69, s51, 0
	s_add_u32 s50, s52, 0x80080
	v_mov_b32_e32 v2, 0
	s_addc_u32 s51, s53, 0
	s_mov_b32 s70, -2
	s_cmp_lg_u32 s101, 0
	s_cbranch_scc1 .Lp1_peel
	v_mov_b32_e32 v3, v2
	v_mov_b32_e32 v4, v2
	v_mov_b32_e32 v5, v2
	v_mov_b32_e32 v6, v2
	v_mov_b32_e32 v7, v2
	v_mov_b32_e32 v8, v2
	v_mov_b32_e32 v9, v2
	v_mov_b32_e32 v18, v2
	v_mov_b32_e32 v19, v2
	v_mov_b32_e32 v20, v2
	v_mov_b32_e32 v21, v2
	v_mov_b32_e32 v22, v2
	v_mov_b32_e32 v23, v2
	v_mov_b32_e32 v24, v2
	v_mov_b32_e32 v25, v2
	v_mov_b32_e32 v34, v2
	v_mov_b32_e32 v35, v2
	v_mov_b32_e32 v36, v2
	v_mov_b32_e32 v37, v2
	v_mov_b32_e32 v38, v2
	v_mov_b32_e32 v39, v2
	v_mov_b32_e32 v40, v2
	v_mov_b32_e32 v41, v2
	v_mov_b32_e32 v50, v2
	v_mov_b32_e32 v51, v2
	v_mov_b32_e32 v52, v2
	v_mov_b32_e32 v53, v2
	v_mov_b32_e32 v54, v2
	v_mov_b32_e32 v55, v2
	v_mov_b32_e32 v56, v2
	v_mov_b32_e32 v57, v2
	v_mov_b32_e32 v10, v2
	v_mov_b32_e32 v11, v2
	v_mov_b32_e32 v12, v2
	v_mov_b32_e32 v13, v2
	v_mov_b32_e32 v14, v2
	v_mov_b32_e32 v15, v2
	v_mov_b32_e32 v16, v2
	v_mov_b32_e32 v17, v2
	v_mov_b32_e32 v26, v2
	v_mov_b32_e32 v27, v2
	v_mov_b32_e32 v28, v2
	v_mov_b32_e32 v29, v2
	v_mov_b32_e32 v30, v2
	v_mov_b32_e32 v31, v2
	v_mov_b32_e32 v32, v2
	v_mov_b32_e32 v33, v2
	v_mov_b32_e32 v42, v2
	v_mov_b32_e32 v43, v2
	v_mov_b32_e32 v44, v2
	v_mov_b32_e32 v45, v2
	v_mov_b32_e32 v46, v2
	v_mov_b32_e32 v47, v2
	v_mov_b32_e32 v48, v2
	v_mov_b32_e32 v49, v2
	v_mov_b32_e32 v58, v2
	v_mov_b32_e32 v59, v2
	v_mov_b32_e32 v60, v2
	v_mov_b32_e32 v61, v2
	v_mov_b32_e32 v62, v2
	v_mov_b32_e32 v63, v2
	v_mov_b32_e32 v64, v2
	v_mov_b32_e32 v65, v2
	v_mov_b32_e32 v66, v2
	v_mov_b32_e32 v67, v2
	v_mov_b32_e32 v68, v2
	v_mov_b32_e32 v69, v2
	v_mov_b32_e32 v70, v2
	v_mov_b32_e32 v71, v2
	v_mov_b32_e32 v72, v2
	v_mov_b32_e32 v73, v2
	v_mov_b32_e32 v82, v2
	v_mov_b32_e32 v83, v2
	v_mov_b32_e32 v84, v2
	v_mov_b32_e32 v85, v2
	v_mov_b32_e32 v86, v2
	v_mov_b32_e32 v87, v2
	v_mov_b32_e32 v88, v2
	v_mov_b32_e32 v89, v2
	v_mov_b32_e32 v98, v2
	v_mov_b32_e32 v99, v2
	v_mov_b32_e32 v100, v2
	v_mov_b32_e32 v101, v2
	v_mov_b32_e32 v102, v2
	v_mov_b32_e32 v103, v2
	v_mov_b32_e32 v104, v2
	v_mov_b32_e32 v105, v2
	v_mov_b32_e32 v114, v2
	v_mov_b32_e32 v115, v2
	v_mov_b32_e32 v116, v2
	v_mov_b32_e32 v117, v2
	v_mov_b32_e32 v118, v2
	v_mov_b32_e32 v119, v2
	v_mov_b32_e32 v120, v2
	v_mov_b32_e32 v121, v2
	v_mov_b32_e32 v74, v2
	v_mov_b32_e32 v75, v2
	v_mov_b32_e32 v76, v2
	v_mov_b32_e32 v77, v2
	v_mov_b32_e32 v78, v2
	v_mov_b32_e32 v79, v2
	v_mov_b32_e32 v80, v2
	v_mov_b32_e32 v81, v2
	v_mov_b32_e32 v90, v2
	v_mov_b32_e32 v91, v2
	v_mov_b32_e32 v92, v2
	v_mov_b32_e32 v93, v2
	v_mov_b32_e32 v94, v2
	v_mov_b32_e32 v95, v2
	v_mov_b32_e32 v96, v2
	v_mov_b32_e32 v97, v2
	v_mov_b32_e32 v106, v2
	v_mov_b32_e32 v107, v2
	v_mov_b32_e32 v108, v2
	v_mov_b32_e32 v109, v2
	v_mov_b32_e32 v110, v2
	v_mov_b32_e32 v111, v2
	v_mov_b32_e32 v112, v2
	v_mov_b32_e32 v113, v2
	v_mov_b32_e32 v122, v2
	v_mov_b32_e32 v123, v2
	v_mov_b32_e32 v124, v2
	v_mov_b32_e32 v125, v2
	v_mov_b32_e32 v126, v2
	v_mov_b32_e32 v127, v2
	v_mov_b32_e32 v128, v2
	v_mov_b32_e32 v129, v2

; #define PG8_BAR __builtin_amdgcn_s_barrier()
; template <class Epi, class Sched, bool GATHER, bool SEGHOOK = false>
; __device__ __forceinline__ void gemm_phase(LAS unsigned char* lds, const int K, const Sched& S, const Epi& E, int tid_) {
;     ...
;         }
;         if (wr == 0) PG8_BAR;
;         E(acc, cur, wr, wc, fr, fq);
;         if (!has_next) break;
.Lp1_loop_exit:
	s_mov_b32 s101, 1
	s_and_b64 vcc, exec, s[10:11]
	s_cbranch_vccz .LBB0_222
	s_barrier

; #define PG8_STAGE_A(bufoff, kptr, h) do { if constexpr (GATHER) { PG8_STAGE(bufoff, kptr, oa[h]); } else { PG8_STAGE(bufoff, (kptr) + (h) * hstep, voffA); } } while (0)
; #define PG8_GATHER_OFFS(uidx) do { _Pragma("unroll") for (int _h = 0; _h < 2; ++_h) _Pragma("unroll") for (int _i = 0; _i < 2; ++_i) \
;         oa[_h][_i] = (unsigned)(S.gather_row((uidx), _h * HALF + _i * 64 + Rst0) * K + Cst0) * 2u; } while (0)
; #define PG8_STAGE(bufoff, gbase, voff) do { _Pragma("unroll") for (int _i = 0; _i < 2; ++_i) \
;         __builtin_amdgcn_global_load_lds((const unsigned*)((const char*)(gbase) + (voff)[_i]), (LAS unsigned*)(lds + (bufoff) + ldsw + _i * 8192), 16, 0, 0); } while (0)
; #define PG8_LDA(dst, b, h) do { _Pragma("unroll") for (int m = 0; m < 4; ++m) _Pragma("unroll") for (int k = 0; k < 2; ++k) dst[m][k] = *(const LAS bf16x8*)(lds + PG8_SA(b, h) + aoff + m * 2048 + k * 1024); } while (0)
; #define PG8_LDB(dst, b, h) do { _Pragma("unroll") for (int n = 0; n < 2; ++n) _Pragma("unroll") for (int k = 0; k < 2; ++k) dst[n][k] = *(const LAS bf16x8*)(lds + PG8_SB(b, h) + boff + n * 2048 + k * 1024); } while (0)
; template <class Epi, class Sched, bool GATHER, bool SEGHOOK = false>
; __device__ __forceinline__ void gemm_phase(LAS unsigned char* lds, const int K, const Sched& S, const Epi& E, int tid_) {
;     ...
;         for (int t = 0; t < nt; t += 2) {
;             const bool last = (t == nt - 2);
;             if constexpr (SEGHOOK) { if (t == 16 || t == 32) E.rescale(acc, cur, t >> 4, wr, wc, fr, fq); }
;             const char* a1 = cA + (size_t)(t + 1) * kstep;
;             const char* a2 = last ? nA : cA + (size_t)(t + 2) * kstep; const char* b2 = last ? nB : cB + (size_t)(t + 2) * kstep;
;             const char* a3 = a2 + kstep; const char* b3 = b2 + kstep;
;             PG8_LDB(B0, 0, 0); PG8_LDB(B1, 0, 1); PG8_SCHED; PG8_LDA(At, 0, 0); PG8_STAGE_A(PG8_SA(1, 1), a1, 1);
;             if constexpr (GATHER) { if (last && has_next) { PG8_GATHER_OFFS(ui + 1); } }
;             PG8_WAIT_V(8); PG8_WAIT_L(0); PG8_BAR; PG8_MMA(0, 0, At, B0); PG8_MMA(0, 1, At, B1); PG8_BAR; PG8_SCHED;
;             PG8_LDA(At, 0, 1); PG8_STAGE(PG8_SB(0, 0), b2, voffB); PG8_STAGE(PG8_SB(0, 1), b2 + hstep, voffB); PG8_STAGE_A(PG8_SA(0, 0), a2, 0);
;             PG8_WAIT_V(8); PG8_WAIT_L(0); PG8_BAR; PG8_MMA(1, 0, At, B0); PG8_MMA(1, 1, At, B1); PG8_BAR; PG8_SCHED;
.Lp1_peel:
	s_add_u32 s9, s50, 0xfff80080
	s_addc_u32 s52, s51, -1
	s_add_i32 s71, 0, 0x10000
	s_cmp_eq_u32 s70, 28
	s_cselect_b32 s55, s8, s52
	s_cselect_b32 s54, s16, s9
	s_cselect_b32 s53, s13, s69
	s_cselect_b32 s52, s39, s41
	s_add_i32 s9, 0, 0x14000
	v_add_u32_e32 v156, s71, v145
	v_add_u32_e32 v172, s9, v145
	ds_read_b128 v[140:143], v156
	ds_read_b128 v[148:151], v156 offset:1024
	ds_read_b128 v[152:155], v156 offset:2048
	ds_read_b128 v[156:159], v156 offset:3072
	ds_read_b128 v[160:163], v172
	ds_read_b128 v[164:167], v172 offset:1024
	ds_read_b128 v[168:171], v172 offset:2048
	ds_read_b128 v[172:175], v172 offset:3072
	v_lshl_add_u64 v[192:193], s[50:51], 0, v[138:139]
	s_add_i32 m0, s49, 0xc000
	ds_read_b128 v[176:179], v147
	ds_read_b128 v[180:183], v147 offset:1024
	ds_read_b128 v[184:187], v147 offset:2048
	ds_read_b128 v[188:191], v147 offset:3072
	ds_read_b128 v[200:203], v147 offset:4096
	ds_read_b128 v[204:207], v147 offset:5120
	ds_read_b128 v[208:211], v147 offset:6144
	ds_read_b128 v[212:215], v147 offset:7168
	global_load_lds_dwordx4 v[192:193], off
	v_lshl_add_u64 v[192:193], s[50:51], 0, v[136:137]
	s_add_i32 m0, s49, 0xe000
	s_nop 0
	global_load_lds_dwordx4 v[192:193], off
	s_waitcnt vmcnt(24)
	s_waitcnt lgkmcnt(0)
	s_barrier
	s_setprio 1
	s_waitcnt lgkmcnt(0)
	v_mfma_f32_16x16x32_bf16 v[126:129], v[140:143], v[176:179], 0
	v_mfma_f32_16x16x32_bf16 v[122:125], v[152:155], v[176:179], 0
	v_mfma_f32_16x16x32_bf16 v[110:113], v[140:143], v[184:187], 0
	v_mfma_f32_16x16x32_bf16 v[106:109], v[152:155], v[184:187], 0
	v_mfma_f32_16x16x32_bf16 v[94:97], v[140:143], v[200:203], 0
	v_mfma_f32_16x16x32_bf16 v[90:93], v[152:155], v[200:203], 0
	v_mfma_f32_16x16x32_bf16 v[78:81], v[140:143], v[208:211], 0
	v_mfma_f32_16x16x32_bf16 v[74:77], v[152:155], v[208:211], 0
	v_mfma_f32_16x16x32_bf16 v[126:129], v[148:151], v[180:183], v[126:129]
	v_mfma_f32_16x16x32_bf16 v[122:125], v[156:159], v[180:183], v[122:125]
	v_mfma_f32_16x16x32_bf16 v[110:113], v[148:151], v[188:191], v[110:113]
	v_mfma_f32_16x16x32_bf16 v[106:109], v[156:159], v[188:191], v[106:109]
	v_mfma_f32_16x16x32_bf16 v[94:97], v[148:151], v[204:207], v[94:97]
	v_mfma_f32_16x16x32_bf16 v[90:93], v[156:159], v[204:207], v[90:93]
	v_mfma_f32_16x16x32_bf16 v[78:81], v[148:151], v[212:215], v[78:81]
	v_mfma_f32_16x16x32_bf16 v[74:77], v[156:159], v[212:215], v[74:77]
	s_setprio 0
	s_setprio 1
	v_mfma_f32_16x16x32_bf16 v[118:121], v[160:163], v[176:179], 0
	v_mfma_f32_16x16x32_bf16 v[114:117], v[168:171], v[176:179], 0
	v_mfma_f32_16x16x32_bf16 v[102:105], v[160:163], v[184:187], 0
	v_mfma_f32_16x16x32_bf16 v[98:101], v[168:171], v[184:187], 0
	v_mfma_f32_16x16x32_bf16 v[86:89], v[160:163], v[200:203], 0
	v_mfma_f32_16x16x32_bf16 v[82:85], v[168:171], v[200:203], 0
	v_mfma_f32_16x16x32_bf16 v[70:73], v[160:163], v[208:211], 0
	v_mfma_f32_16x16x32_bf16 v[66:69], v[168:171], v[208:211], 0
	v_mfma_f32_16x16x32_bf16 v[118:121], v[164:167], v[180:183], v[118:121]
	v_mfma_f32_16x16x32_bf16 v[114:117], v[172:175], v[180:183], v[114:117]
	v_mfma_f32_16x16x32_bf16 v[102:105], v[164:167], v[188:191], v[102:105]
	v_mfma_f32_16x16x32_bf16 v[98:101], v[172:175], v[188:191], v[98:101]
	v_mfma_f32_16x16x32_bf16 v[86:89], v[164:167], v[204:207], v[86:89]
	v_mfma_f32_16x16x32_bf16 v[82:85], v[172:175], v[204:207], v[82:85]
	v_mfma_f32_16x16x32_bf16 v[70:73], v[164:167], v[212:215], v[70:73]
	v_mfma_f32_16x16x32_bf16 v[66:69], v[172:175], v[212:215], v[66:69]
	s_setprio 0
	s_barrier
	s_add_i32 s71, s71, s62
	v_lshl_add_u64 v[192:193], s[52:53], 0, v[0:1]
	s_mov_b32 m0, s71
	ds_read_b128 v[176:179], v147 offset:16384
	ds_read_b128 v[180:183], v147 offset:17408
	ds_read_b128 v[184:187], v147 offset:18432
	ds_read_b128 v[188:191], v147 offset:19456
	ds_read_b128 v[200:203], v147 offset:20480
	ds_read_b128 v[204:207], v147 offset:21504
	ds_read_b128 v[208:211], v147 offset:22528
	ds_read_b128 v[212:215], v147 offset:23552
	global_load_lds_dwordx4 v[192:193], off
	s_add_i32 m0, s71, 0x2000
	s_add_u32 s78, s52, 0x80000
	v_lshl_add_u64 v[216:217], s[52:53], 0, v[134:135]
	s_addc_u32 s79, s53, 0
	s_add_i32 s9, s9, s62
	global_load_lds_dwordx4 v[216:217], off
	v_lshl_add_u64 v[218:219], s[78:79], 0, v[0:1]
	s_mov_b32 m0, s9
	v_lshl_add_u64 v[220:221], s[54:55], 0, v[132:133]
	global_load_lds_dwordx4 v[218:219], off
	v_lshl_add_u64 v[218:219], s[78:79], 0, v[134:135]
	s_add_i32 m0, s9, 0x2000
	s_nop 0
	global_load_lds_dwordx4 v[218:219], off
	v_lshl_add_u64 v[218:219], s[54:55], 0, v[130:131]
	s_mov_b32 m0, s49
	s_nop 0
	global_load_lds_dwordx4 v[218:219], off
	s_mov_b32 m0, s63
	s_nop 0
	global_load_lds_dwordx4 v[220:221], off
	s_waitcnt vmcnt(24)
	s_waitcnt lgkmcnt(0)
	s_barrier
; #define PG8_STAGE_A(bufoff, kptr, h) do { if constexpr (GATHER) { PG8_STAGE(bufoff, kptr, oa[h]); } else { PG8_STAGE(bufoff, (kptr) + (h) * hstep, voffA); } } while (0)
; #define PG8_LDA(dst, b, h) do { _Pragma("unroll") for (int m = 0; m < 4; ++m) _Pragma("unroll") for (int k = 0; k < 2; ++k) dst[m][k] = *(const LAS bf16x8*)(lds + PG8_SA(b, h) + aoff + m * 2048 + k * 1024); } while (0)
; #define PG8_LDB(dst, b, h) do { _Pragma("unroll") for (int n = 0; n < 2; ++n) _Pragma("unroll") for (int k = 0; k < 2; ++k) dst[n][k] = *(const LAS bf16x8*)(lds + PG8_SB(b, h) + boff + n * 2048 + k * 1024); } while (0)
; #define PG8_MMA(ai, bj, At, Bt) do { __builtin_amdgcn_s_setprio(1); _Pragma("unroll") for (int m = 0; m < 4; ++m) _Pragma("unroll") for (int n = 0; n < 2; ++n) _Pragma("unroll") for (int k = 0; k < 2; ++k) \
;         acc[ai][bj][m][n] = __builtin_amdgcn_mfma_f32_16x16x32_bf16(Bt[n][k], At[m][k], acc[ai][bj][m][n], 0, 0, 0); __builtin_amdgcn_s_setprio(0); } while (0)
; #define PG8_WAIT_V(n) asm volatile("s_waitcnt vmcnt(" #n ")" ::: "memory")
; #define PG8_WAIT_L(n) asm volatile("s_waitcnt lgkmcnt(" #n ")" ::: "memory")
; #define PG8_BAR __builtin_amdgcn_s_barrier()
; #define PG8_SCHED __builtin_amdgcn_sched_barrier(0)
; template <class Epi, class Sched, bool GATHER, bool SEGHOOK = false>
; __device__ __forceinline__ void gemm_phase(LAS unsigned char* lds, const int K, const Sched& S, const Epi& E, int tid_) {
;     ...
;             PG8_WAIT_V(8); PG8_WAIT_L(0); PG8_BAR; PG8_MMA(1, 0, At, B0); PG8_MMA(1, 1, At, B1); PG8_BAR; PG8_SCHED;
;             PG8_LDB(B0, 1, 0); PG8_LDB(B1, 1, 1); PG8_SCHED; PG8_LDA(At, 1, 0); PG8_STAGE_A(PG8_SA(0, 1), a2, 1);
;             PG8_WAIT_V(8); PG8_WAIT_L(0); PG8_BAR; PG8_MMA(0, 0, At, B0); PG8_MMA(0, 1, At, B1); PG8_BAR; PG8_SCHED;
	s_setprio 1
	s_waitcnt lgkmcnt(0)
	v_mfma_f32_16x16x32_bf16 v[62:65], v[140:143], v[176:179], 0
	v_mfma_f32_16x16x32_bf16 v[58:61], v[152:155], v[176:179], 0
	v_mfma_f32_16x16x32_bf16 v[46:49], v[140:143], v[184:187], 0
	v_mfma_f32_16x16x32_bf16 v[42:45], v[152:155], v[184:187], 0
	v_mfma_f32_16x16x32_bf16 v[30:33], v[140:143], v[200:203], 0
	v_mfma_f32_16x16x32_bf16 v[26:29], v[152:155], v[200:203], 0
	v_mfma_f32_16x16x32_bf16 v[14:17], v[140:143], v[208:211], 0
	v_mfma_f32_16x16x32_bf16 v[10:13], v[152:155], v[208:211], 0
	v_mfma_f32_16x16x32_bf16 v[62:65], v[148:151], v[180:183], v[62:65]
	v_mfma_f32_16x16x32_bf16 v[58:61], v[156:159], v[180:183], v[58:61]
	v_mfma_f32_16x16x32_bf16 v[46:49], v[148:151], v[188:191], v[46:49]
	v_mfma_f32_16x16x32_bf16 v[42:45], v[156:159], v[188:191], v[42:45]
	v_mfma_f32_16x16x32_bf16 v[30:33], v[148:151], v[204:207], v[30:33]
	v_mfma_f32_16x16x32_bf16 v[26:29], v[156:159], v[204:207], v[26:29]
	v_mfma_f32_16x16x32_bf16 v[14:17], v[148:151], v[212:215], v[14:17]
	v_mfma_f32_16x16x32_bf16 v[10:13], v[156:159], v[212:215], v[10:13]
	s_setprio 0
	s_setprio 1
	v_mfma_f32_16x16x32_bf16 v[54:57], v[160:163], v[176:179], 0
	v_mfma_f32_16x16x32_bf16 v[50:53], v[168:171], v[176:179], 0
	v_mfma_f32_16x16x32_bf16 v[38:41], v[160:163], v[184:187], 0
	v_mfma_f32_16x16x32_bf16 v[34:37], v[168:171], v[184:187], 0
	v_mfma_f32_16x16x32_bf16 v[22:25], v[160:163], v[200:203], 0
	v_mfma_f32_16x16x32_bf16 v[18:21], v[168:171], v[200:203], 0
	v_mfma_f32_16x16x32_bf16 v[6:9], v[160:163], v[208:211], 0
	v_mfma_f32_16x16x32_bf16 v[2:5], v[168:171], v[208:211], 0
	v_mfma_f32_16x16x32_bf16 v[54:57], v[164:167], v[180:183], v[54:57]
	v_mfma_f32_16x16x32_bf16 v[50:53], v[172:175], v[180:183], v[50:53]
	v_mfma_f32_16x16x32_bf16 v[38:41], v[164:167], v[188:191], v[38:41]
	v_mfma_f32_16x16x32_bf16 v[34:37], v[172:175], v[188:191], v[34:37]
	v_mfma_f32_16x16x32_bf16 v[22:25], v[164:167], v[204:207], v[22:25]
	v_mfma_f32_16x16x32_bf16 v[18:21], v[172:175], v[204:207], v[18:21]
	v_mfma_f32_16x16x32_bf16 v[6:9], v[164:167], v[212:215], v[6:9]
	v_mfma_f32_16x16x32_bf16 v[2:5], v[172:175], v[212:215], v[2:5]
	s_setprio 0
	s_barrier
	s_add_i32 s9, 0, 0x18000
	s_add_i32 s71, 0, 0x1c000
	v_add_u32_e32 v156, s9, v145
	v_add_u32_e32 v172, s71, v145
	ds_read_b128 v[140:143], v156
	ds_read_b128 v[148:151], v156 offset:1024
	ds_read_b128 v[152:155], v156 offset:2048
	ds_read_b128 v[156:159], v156 offset:3072
	ds_read_b128 v[160:163], v172
	ds_read_b128 v[164:167], v172 offset:1024
	ds_read_b128 v[168:171], v172 offset:2048
	ds_read_b128 v[172:175], v172 offset:3072
	s_add_u32 s54, s54, 0x80000
	s_addc_u32 s55, s55, 0
	s_mov_b32 m0, s64
	v_lshl_add_u64 v[236:237], s[54:55], 0, v[130:131]
	ds_read_b128 v[176:179], v147 offset:32768
	ds_read_b128 v[180:183], v147 offset:33792
	ds_read_b128 v[184:187], v147 offset:34816
	ds_read_b128 v[188:191], v147 offset:35840
	ds_read_b128 v[200:203], v147 offset:36864
	ds_read_b128 v[204:207], v147 offset:37888
	ds_read_b128 v[208:211], v147 offset:38912
	ds_read_b128 v[212:215], v147 offset:39936
	global_load_lds_dwordx4 v[236:237], off
	v_lshl_add_u64 v[236:237], s[54:55], 0, v[132:133]
	s_mov_b32 m0, s65
	s_nop 0
	global_load_lds_dwordx4 v[236:237], off
	s_waitcnt vmcnt(8)
	s_waitcnt lgkmcnt(0)
	s_barrier
	s_setprio 1
	s_waitcnt lgkmcnt(0)
	v_mfma_f32_16x16x32_bf16 v[126:129], v[140:143], v[176:179], v[126:129]
	v_mfma_f32_16x16x32_bf16 v[122:125], v[152:155], v[176:179], v[122:125]
	v_mfma_f32_16x16x32_bf16 v[110:113], v[140:143], v[184:187], v[110:113]
	v_mfma_f32_16x16x32_bf16 v[106:109], v[152:155], v[184:187], v[106:109]
	v_mfma_f32_16x16x32_bf16 v[94:97], v[140:143], v[200:203], v[94:97]
	v_mfma_f32_16x16x32_bf16 v[90:93], v[152:155], v[200:203], v[90:93]
	v_mfma_f32_16x16x32_bf16 v[78:81], v[140:143], v[208:211], v[78:81]
	v_mfma_f32_16x16x32_bf16 v[74:77], v[152:155], v[208:211], v[74:77]
	v_mfma_f32_16x16x32_bf16 v[126:129], v[148:151], v[180:183], v[126:129]
	v_mfma_f32_16x16x32_bf16 v[122:125], v[156:159], v[180:183], v[122:125]
	v_mfma_f32_16x16x32_bf16 v[110:113], v[148:151], v[188:191], v[110:113]
	v_mfma_f32_16x16x32_bf16 v[106:109], v[156:159], v[188:191], v[106:109]
	v_mfma_f32_16x16x32_bf16 v[94:97], v[148:151], v[204:207], v[94:97]
	v_mfma_f32_16x16x32_bf16 v[90:93], v[156:159], v[204:207], v[90:93]
	v_mfma_f32_16x16x32_bf16 v[78:81], v[148:151], v[212:215], v[78:81]
	v_mfma_f32_16x16x32_bf16 v[74:77], v[156:159], v[212:215], v[74:77]
	s_setprio 0
	s_setprio 1
	v_mfma_f32_16x16x32_bf16 v[118:121], v[160:163], v[176:179], v[118:121]
	v_mfma_f32_16x16x32_bf16 v[114:117], v[168:171], v[176:179], v[114:117]
	v_mfma_f32_16x16x32_bf16 v[102:105], v[160:163], v[184:187], v[102:105]
	v_mfma_f32_16x16x32_bf16 v[98:101], v[168:171], v[184:187], v[98:101]
	v_mfma_f32_16x16x32_bf16 v[86:89], v[160:163], v[200:203], v[86:89]
	v_mfma_f32_16x16x32_bf16 v[82:85], v[168:171], v[200:203], v[82:85]
	v_mfma_f32_16x16x32_bf16 v[70:73], v[160:163], v[208:211], v[70:73]
	v_mfma_f32_16x16x32_bf16 v[66:69], v[168:171], v[208:211], v[66:69]
	v_mfma_f32_16x16x32_bf16 v[118:121], v[164:167], v[180:183], v[118:121]
	v_mfma_f32_16x16x32_bf16 v[114:117], v[172:175], v[180:183], v[114:117]
	v_mfma_f32_16x16x32_bf16 v[102:105], v[164:167], v[188:191], v[102:105]
	v_mfma_f32_16x16x32_bf16 v[98:101], v[172:175], v[188:191], v[98:101]
	v_mfma_f32_16x16x32_bf16 v[86:89], v[164:167], v[204:207], v[86:89]
	v_mfma_f32_16x16x32_bf16 v[82:85], v[172:175], v[204:207], v[82:85]
	v_mfma_f32_16x16x32_bf16 v[70:73], v[164:167], v[212:215], v[70:73]
	v_mfma_f32_16x16x32_bf16 v[66:69], v[172:175], v[212:215], v[66:69]
	s_setprio 0
	s_barrier
; #define PG8_STAGE_A(bufoff, kptr, h) do { if constexpr (GATHER) { PG8_STAGE(bufoff, kptr, oa[h]); } else { PG8_STAGE(bufoff, (kptr) + (h) * hstep, voffA); } } while (0)
; #define PG8_STAGE(bufoff, gbase, voff) do { _Pragma("unroll") for (int _i = 0; _i < 2; ++_i) \
;         __builtin_amdgcn_global_load_lds((const unsigned*)((const char*)(gbase) + (voff)[_i]), (LAS unsigned*)(lds + (bufoff) + ldsw + _i * 8192), 16, 0, 0); } while (0)
; #define PG8_LDA(dst, b, h) do { _Pragma("unroll") for (int m = 0; m < 4; ++m) _Pragma("unroll") for (int k = 0; k < 2; ++k) dst[m][k] = *(const LAS bf16x8*)(lds + PG8_SA(b, h) + aoff + m * 2048 + k * 1024); } while (0)
; #define PG8_MMA(ai, bj, At, Bt) do { __builtin_amdgcn_s_setprio(1); _Pragma("unroll") for (int m = 0; m < 4; ++m) _Pragma("unroll") for (int n = 0; n < 2; ++n) _Pragma("unroll") for (int k = 0; k < 2; ++k) \
;         acc[ai][bj][m][n] = __builtin_amdgcn_mfma_f32_16x16x32_bf16(Bt[n][k], At[m][k], acc[ai][bj][m][n], 0, 0, 0); __builtin_amdgcn_s_setprio(0); } while (0)
; #define PG8_WAIT_V(n) asm volatile("s_waitcnt vmcnt(" #n ")" ::: "memory")
; #define PG8_WAIT_L(n) asm volatile("s_waitcnt lgkmcnt(" #n ")" ::: "memory")
; #define PG8_BAR __builtin_amdgcn_s_barrier()
; #define PG8_SCHED __builtin_amdgcn_sched_barrier(0)
; template <class Epi, class Sched, bool GATHER, bool SEGHOOK = false>
; __device__ __forceinline__ void gemm_phase(LAS unsigned char* lds, const int K, const Sched& S, const Epi& E, int tid_) {
;     ...
;             PG8_LDA(At, 1, 1); PG8_STAGE(PG8_SB(1, 0), b3, voffB); PG8_STAGE(PG8_SB(1, 1), b3 + hstep, voffB); PG8_STAGE_A(PG8_SA(1, 0), a3, 0);
;             PG8_WAIT_V(8); PG8_WAIT_L(0); PG8_BAR; PG8_MMA(1, 0, At, B0); PG8_MMA(1, 1, At, B1); PG8_BAR; PG8_SCHED;
;         }
	s_add_i32 s9, s9, s62
	v_lshl_add_u64 v[192:193], v[192:193], 0, s[90:91]
	s_mov_b32 m0, s9
	ds_read_b128 v[176:179], v147 offset:49152
	ds_read_b128 v[180:183], v147 offset:50176
	ds_read_b128 v[184:187], v147 offset:51200
	ds_read_b128 v[188:191], v147 offset:52224
	ds_read_b128 v[200:203], v147 offset:53248
	ds_read_b128 v[204:207], v147 offset:54272
	ds_read_b128 v[208:211], v147 offset:55296
	ds_read_b128 v[212:215], v147 offset:56320
	global_load_lds_dwordx4 v[192:193], off
	s_add_i32 m0, s9, 0x2000
	s_add_u32 s52, s52, 0x80080
	v_lshl_add_u64 v[192:193], v[216:217], 0, s[90:91]
	s_addc_u32 s53, s53, 0
	s_add_i32 s9, s71, s62
	global_load_lds_dwordx4 v[192:193], off
	v_lshl_add_u64 v[192:193], s[52:53], 0, v[0:1]
	s_mov_b32 m0, s9
	s_nop 0
	global_load_lds_dwordx4 v[192:193], off
	v_lshl_add_u64 v[192:193], s[52:53], 0, v[134:135]
	s_add_i32 m0, s9, 0x2000
	s_nop 0
	global_load_lds_dwordx4 v[192:193], off
	v_lshl_add_u64 v[192:193], v[218:219], 0, s[90:91]
	s_mov_b32 m0, s66
	s_nop 0
	global_load_lds_dwordx4 v[192:193], off
	v_lshl_add_u64 v[192:193], v[220:221], 0, s[90:91]
	s_mov_b32 m0, s67
	s_nop 0
	global_load_lds_dwordx4 v[192:193], off
	s_waitcnt vmcnt(8)
	s_waitcnt lgkmcnt(0)
	s_barrier
	s_setprio 1
	s_waitcnt lgkmcnt(0)
	v_mfma_f32_16x16x32_bf16 v[62:65], v[140:143], v[176:179], v[62:65]
	v_mfma_f32_16x16x32_bf16 v[58:61], v[152:155], v[176:179], v[58:61]
	v_mfma_f32_16x16x32_bf16 v[46:49], v[140:143], v[184:187], v[46:49]
	v_mfma_f32_16x16x32_bf16 v[42:45], v[152:155], v[184:187], v[42:45]
	v_mfma_f32_16x16x32_bf16 v[30:33], v[140:143], v[200:203], v[30:33]
	v_mfma_f32_16x16x32_bf16 v[26:29], v[152:155], v[200:203], v[26:29]
	v_mfma_f32_16x16x32_bf16 v[14:17], v[140:143], v[208:211], v[14:17]
	v_mfma_f32_16x16x32_bf16 v[10:13], v[152:155], v[208:211], v[10:13]
	v_mfma_f32_16x16x32_bf16 v[62:65], v[148:151], v[180:183], v[62:65]
	v_mfma_f32_16x16x32_bf16 v[58:61], v[156:159], v[180:183], v[58:61]
	v_mfma_f32_16x16x32_bf16 v[46:49], v[148:151], v[188:191], v[46:49]
	v_mfma_f32_16x16x32_bf16 v[42:45], v[156:159], v[188:191], v[42:45]
	v_mfma_f32_16x16x32_bf16 v[30:33], v[148:151], v[204:207], v[30:33]
	v_mfma_f32_16x16x32_bf16 v[26:29], v[156:159], v[204:207], v[26:29]
	v_mfma_f32_16x16x32_bf16 v[14:17], v[148:151], v[212:215], v[14:17]
	v_mfma_f32_16x16x32_bf16 v[10:13], v[156:159], v[212:215], v[10:13]
	s_setprio 0
	s_setprio 1
	v_mfma_f32_16x16x32_bf16 v[54:57], v[160:163], v[176:179], v[54:57]
	v_mfma_f32_16x16x32_bf16 v[50:53], v[168:171], v[176:179], v[50:53]
	v_mfma_f32_16x16x32_bf16 v[38:41], v[160:163], v[184:187], v[38:41]
	v_mfma_f32_16x16x32_bf16 v[34:37], v[168:171], v[184:187], v[34:37]
	v_mfma_f32_16x16x32_bf16 v[22:25], v[160:163], v[200:203], v[22:25]
	v_mfma_f32_16x16x32_bf16 v[18:21], v[168:171], v[200:203], v[18:21]
	v_mfma_f32_16x16x32_bf16 v[6:9], v[160:163], v[208:211], v[6:9]
	v_mfma_f32_16x16x32_bf16 v[2:5], v[168:171], v[208:211], v[2:5]
	v_mfma_f32_16x16x32_bf16 v[54:57], v[164:167], v[180:183], v[54:57]
	v_mfma_f32_16x16x32_bf16 v[50:53], v[172:175], v[180:183], v[50:53]
	v_mfma_f32_16x16x32_bf16 v[38:41], v[164:167], v[188:191], v[38:41]
	v_mfma_f32_16x16x32_bf16 v[34:37], v[172:175], v[188:191], v[34:37]
	v_mfma_f32_16x16x32_bf16 v[22:25], v[164:167], v[204:207], v[22:25]
	v_mfma_f32_16x16x32_bf16 v[18:21], v[172:175], v[204:207], v[18:21]
	v_mfma_f32_16x16x32_bf16 v[6:9], v[164:167], v[212:215], v[6:9]
	v_mfma_f32_16x16x32_bf16 v[2:5], v[172:175], v[212:215], v[2:5]
	s_setprio 0
	s_barrier
	s_add_i32 s70, s70, 2
	s_add_u32 s41, s41, 0x100
	s_addc_u32 s69, s69, 0
	s_add_u32 s50, s50, 0x100
	s_addc_u32 s51, s51, 0
	s_cmp_gt_u32 s70, 29
	s_cbranch_scc0 .LBB0_219
	s_branch .Lp1_loop_exit

; template <unsigned PHMASK> __global__ void __launch_bounds__(NTHR, 2) fwd(Args args) {
	.amdhsa_kernel _Z3fwdILj4095EEv4Args
		.amdhsa_group_segment_fixed_size 0
		.amdhsa_private_segment_fixed_size 0
		.amdhsa_kernarg_size 496
		.amdhsa_user_sgpr_count 2
		.amdhsa_user_sgpr_dispatch_ptr 0
		.amdhsa_user_sgpr_queue_ptr 0
		.amdhsa_user_sgpr_kernarg_segment_ptr 1
		.amdhsa_user_sgpr_dispatch_id 0
		.amdhsa_user_sgpr_kernarg_preload_length 0
		.amdhsa_user_sgpr_kernarg_preload_offset 0
		.amdhsa_user_sgpr_private_segment_size 0
		.amdhsa_uses_dynamic_stack 0
		.amdhsa_enable_private_segment 0
		.amdhsa_system_sgpr_workgroup_id_x 1
		.amdhsa_system_sgpr_workgroup_id_y 0
		.amdhsa_system_sgpr_workgroup_id_z 0
		.amdhsa_system_sgpr_workgroup_info 0
		.amdhsa_system_vgpr_workitem_id 0
		.amdhsa_next_free_vgpr 250
		.amdhsa_next_free_sgpr 102
		.amdhsa_accum_offset 252
		.amdhsa_reserve_vcc 1
		.amdhsa_float_round_mode_32 0
		.amdhsa_float_round_mode_16_64 0
		.amdhsa_float_denorm_mode_32 3
		.amdhsa_float_denorm_mode_16_64 3
		.amdhsa_dx10_clamp 1
		.amdhsa_ieee_mode 1
		.amdhsa_fp16_overflow 0
		.amdhsa_tg_split 0
		.amdhsa_exception_fp_ieee_invalid_op 0
		.amdhsa_exception_fp_denorm_src 0
		.amdhsa_exception_fp_ieee_div_zero 0
		.amdhsa_exception_fp_ieee_overflow 0
		.amdhsa_exception_fp_ieee_underflow 0
		.amdhsa_exception_fp_ieee_inexact 0
		.amdhsa_exception_int_div_zero 0
	.end_amdhsa_kernel

; template <unsigned PHMASK> __global__ void __launch_bounds__(NTHR, 2) fwd(Args args) {
amdhsa.kernels:
  - .agpr_count:     0
    .args:
      - .offset:         0
        .size:           240
        .value_kind:     by_value
      - .offset:         240
        .size:           4
        .value_kind:     hidden_block_count_x
      - .offset:         244
        .size:           4
        .value_kind:     hidden_block_count_y
      - .offset:         248
        .size:           4
        .value_kind:     hidden_block_count_z
      - .offset:         252
        .size:           2
        .value_kind:     hidden_group_size_x
      - .offset:         254
        .size:           2
        .value_kind:     hidden_group_size_y
      - .offset:         256
        .size:           2
        .value_kind:     hidden_group_size_z
      - .offset:         258
        .size:           2
        .value_kind:     hidden_remainder_x
      - .offset:         260
        .size:           2
        .value_kind:     hidden_remainder_y
      - .offset:         262
        .size:           2
        .value_kind:     hidden_remainder_z
      - .offset:         280
        .size:           8
        .value_kind:     hidden_global_offset_x
      - .offset:         288
        .size:           8
        .value_kind:     hidden_global_offset_y
      - .offset:         296
        .size:           8
        .value_kind:     hidden_global_offset_z
      - .offset:         304
        .size:           2
        .value_kind:     hidden_grid_dims
      - .offset:         360
        .size:           4
        .value_kind:     hidden_dynamic_lds_size
    .group_segment_fixed_size: 0
    .kernarg_segment_align: 8
    .kernarg_segment_size: 496
    .language:       OpenCL C
    .language_version:
      - 2
      - 0
    .max_flat_workgroup_size: 512
    .name:           _Z3fwdILj4095EEv4Args
    .private_segment_fixed_size: 0
    .sgpr_count:     108
    .sgpr_spill_count: 271
    .symbol:         _Z3fwdILj4095EEv4Args.kd
    .uniform_work_group_size: 1
    .uses_dynamic_stack: false
    .vgpr_count:     250
    .vgpr_spill_count: 0
    .wavefront_size: 64
